# attention output stores with the default cache policy instead of nt (the norm phase re-reads them)
# baseline (speedup 1.0000x reference)
; __device__ __forceinline__ unsigned cvtpk(float lo, float hi) { f32x2_t v = {lo, hi}; bf16x2_t b = __builtin_convertvector(v, bf16x2_t); return __builtin_bit_cast(unsigned, b); }
; __device__ __forceinline__ int crow(int r, int hi) { return (r & 3) + 8 * (r >> 2) + 4 * hi; }
; template <class BIAS>
; __device__ __forceinline__ void attn_tiles(char* shm, const UnitIO& io, int t_begin, int t_end, const BIAS& B, int tid) {
;     ...
;     { auto rr = __builtin_amdgcn_permlane32_swap(__float_as_uint(l_reg), __float_as_uint(l_reg), false, false); l_reg = __uint_as_float(rr[0]) + __uint_as_float(rr[1]); }
;     if (hi == 0) wsf[32 + r32] = l_reg;
;     asm volatile("s_waitcnt lgkmcnt(0)" ::: "memory");
;     float rli[16];
; #pragma unroll
;     for (int r = 0; r < 16; ++r) rli[r] = io.norm ? __builtin_amdgcn_rcpf(wsf[32 + crow(r, hi)]) : 1.0f;
;     if (!io.norm && hi == 0) io.L[(long)r32 * io.lstride] = l_reg;
;     { bf16* stg = (bf16*)(shm + LDS_OST) + wid * 2048;
; #pragma unroll
;       for (int r = 0; r < 16; ++r) { const int orow = crow(r, hi);
; #pragma unroll
;           for (int d0 = 0; d0 < 2; ++d0) stg[orow * 64 + d0 * 32 + r32] = (bf16)(cvtpk(o[d0][r] * rli[r], 0.f) & 0xffffu); }
;       asm volatile("s_waitcnt lgkmcnt(0)" ::: "memory");
; #pragma unroll
;       for (int i = 0; i < 4; ++i) { const int row = i * 8 + (lane >> 3), ch = lane & 7; const u32x4 v = *(const u32x4*)(stg + row * 64 + ch * 8); __builtin_nontemporal_store(v, (u32x4*)(io.O + (long)row * io.ostride + ch * 8)); } }
;     asm volatile("s_waitcnt lgkmcnt(0)" ::: "memory");
.LBB0_277:
	s_or_b64 exec, exec, s[4:5]
	s_waitcnt lgkmcnt(0)
	v_add_u32_e32 v42, s12, v155
	ds_read_b128 v[34:37], v42 offset:128
	ds_read_b128 v[38:41], v42 offset:160
	s_lshl_b64 s[4:5], s[10:11], 1
	v_readlane_b32 s10, v254, 61
	s_add_u32 s4, s10, s4
	s_waitcnt lgkmcnt(1)
	v_rcp_f32_e32 v43, v34
	s_addc_u32 s5, s25, s5
	s_lshl_b32 s10, s16, 12
	s_add_i32 s10, s10, 0x10800
	v_rcp_f32_e32 v44, v35
	v_rcp_f32_e32 v45, v36
	v_rcp_f32_e32 v46, v37
	s_waitcnt lgkmcnt(0)
	v_rcp_f32_e32 v47, v38
	ds_read_b128 v[34:37], v42 offset:192
	v_rcp_f32_e32 v48, v39
	v_rcp_f32_e32 v49, v40
	v_rcp_f32_e32 v50, v41
	ds_read_b128 v[38:41], v42 offset:224
	v_mul_f32_e32 v2, v2, v43
	v_lshl_or_b32 v42, v179, 1, s10
	v_cvt_pk_bf16_f32 v2, v2, s0
	v_lshl_add_u32 v42, v146, 1, v42
	ds_write_b16 v42, v2
	v_mul_f32_e32 v2, v18, v43
	v_cvt_pk_bf16_f32 v2, v2, s0
	ds_write_b16 v42, v2 offset:64
	v_mul_f32_e32 v2, v3, v44
	v_cvt_pk_bf16_f32 v2, v2, s0
	ds_write_b16 v42, v2 offset:128
	v_mul_f32_e32 v2, v19, v44
	v_cvt_pk_bf16_f32 v2, v2, s0
	ds_write_b16 v42, v2 offset:192
	v_mul_f32_e32 v2, v4, v45
	v_cvt_pk_bf16_f32 v2, v2, s0
	ds_write_b16 v42, v2 offset:256
	v_mul_f32_e32 v2, v20, v45
	v_cvt_pk_bf16_f32 v2, v2, s0
	ds_write_b16 v42, v2 offset:320
	v_mul_f32_e32 v2, v5, v46
	v_cvt_pk_bf16_f32 v2, v2, s0
	ds_write_b16 v42, v2 offset:384
	v_mul_f32_e32 v2, v21, v46
	v_cvt_pk_bf16_f32 v2, v2, s0
	ds_write_b16 v42, v2 offset:448
	v_mul_f32_e32 v2, v6, v47
	v_cvt_pk_bf16_f32 v2, v2, s0
	ds_write_b16 v42, v2 offset:1024
	v_mul_f32_e32 v2, v22, v47
	v_cvt_pk_bf16_f32 v2, v2, s0
	ds_write_b16 v42, v2 offset:1088
	v_mul_f32_e32 v2, v7, v48
	v_cvt_pk_bf16_f32 v2, v2, s0
	ds_write_b16 v42, v2 offset:1152
	v_mul_f32_e32 v2, v23, v48
	v_cvt_pk_bf16_f32 v2, v2, s0
	ds_write_b16 v42, v2 offset:1216
	v_mul_f32_e32 v2, v8, v49
	v_cvt_pk_bf16_f32 v2, v2, s0
	ds_write_b16 v42, v2 offset:1280
	v_mul_f32_e32 v2, v24, v49
	v_cvt_pk_bf16_f32 v2, v2, s0
	s_waitcnt lgkmcnt(14)
	v_rcp_f32_e32 v34, v34
	ds_write_b16 v42, v2 offset:1344
	v_mul_f32_e32 v2, v9, v50
	v_cvt_pk_bf16_f32 v2, v2, s0
	ds_write_b16 v42, v2 offset:1408
	v_mul_f32_e32 v2, v25, v50
	v_cvt_pk_bf16_f32 v2, v2, s0
	v_rcp_f32_e32 v35, v35
	ds_write_b16 v42, v2 offset:1472
	v_mul_f32_e32 v2, v10, v34
	v_cvt_pk_bf16_f32 v2, v2, s0
	ds_write_b16 v42, v2 offset:2048
	v_mul_f32_e32 v2, v26, v34
	v_cvt_pk_bf16_f32 v2, v2, s0
	v_rcp_f32_e32 v36, v36
	ds_write_b16 v42, v2 offset:2112
	v_mul_f32_e32 v2, v11, v35
	v_cvt_pk_bf16_f32 v2, v2, s0
	ds_write_b16 v42, v2 offset:2176
	v_mul_f32_e32 v2, v27, v35
	v_cvt_pk_bf16_f32 v2, v2, s0
	v_rcp_f32_e32 v37, v37
	ds_write_b16 v42, v2 offset:2240
	v_mul_f32_e32 v2, v12, v36
	v_cvt_pk_bf16_f32 v2, v2, s0
	ds_write_b16 v42, v2 offset:2304
	v_mul_f32_e32 v2, v28, v36
	v_cvt_pk_bf16_f32 v2, v2, s0
	s_waitcnt lgkmcnt(14)
	v_rcp_f32_e32 v38, v38
	ds_write_b16 v42, v2 offset:2368
	v_mul_f32_e32 v2, v13, v37
	v_cvt_pk_bf16_f32 v2, v2, s0
	ds_write_b16 v42, v2 offset:2432
	v_mul_f32_e32 v2, v29, v37
	v_cvt_pk_bf16_f32 v2, v2, s0
	v_rcp_f32_e32 v39, v39
	ds_write_b16 v42, v2 offset:2496
	v_mul_f32_e32 v2, v14, v38
	v_cvt_pk_bf16_f32 v2, v2, s0
	ds_write_b16 v42, v2 offset:3072
	v_mul_f32_e32 v2, v30, v38
	v_cvt_pk_bf16_f32 v2, v2, s0
	v_rcp_f32_e32 v40, v40
	ds_write_b16 v42, v2 offset:3136
	v_mul_f32_e32 v2, v15, v39
	v_cvt_pk_bf16_f32 v2, v2, s0
	ds_write_b16 v42, v2 offset:3200
	v_mul_f32_e32 v2, v31, v39
	v_cvt_pk_bf16_f32 v2, v2, s0
	v_rcp_f32_e32 v41, v41
	ds_write_b16 v42, v2 offset:3264
	v_mul_f32_e32 v2, v16, v40
	v_cvt_pk_bf16_f32 v2, v2, s0
	ds_write_b16 v42, v2 offset:3328
	v_mul_f32_e32 v2, v32, v40
	v_cvt_pk_bf16_f32 v2, v2, s0
	ds_write_b16 v42, v2 offset:3392
	v_mul_f32_e32 v2, v17, v41
	v_cvt_pk_bf16_f32 v2, v2, s0
	ds_write_b16 v42, v2 offset:3456
	v_mul_f32_e32 v2, v33, v41
	v_cvt_pk_bf16_f32 v2, v2, s0
	v_lshlrev_b32_e32 v152, 1, v160
	ds_write_b16 v42, v2 offset:3520
	v_or_b32_e32 v8, s10, v152
	s_waitcnt lgkmcnt(0)
	v_add_u32_e32 v2, v8, v183
	ds_read_b128 v[2:5], v2
	v_lshl_add_u64 v[6:7], s[4:5], 0, v[0:1]
	v_mov_b32_e32 v153, v1
	v_lshl_add_u64 v[6:7], v[6:7], 0, v[152:153]
	v_mov_b32_e32 v135, v1
	s_waitcnt lgkmcnt(0)
	global_store_dwordx4 v[6:7], v[2:5], off
	v_lshl_add_u64 v[6:7], s[4:5], 0, v[134:135]
	v_lshl_add_u64 v[6:7], v[6:7], 0, v[152:153]
	v_add_u32_e32 v2, v8, v185
	ds_read_b128 v[2:5], v2
	v_mov_b32_e32 v137, v1
	v_mov_b32_e32 v139, v1
	s_and_b64 vcc, exec, s[8:9]
	s_waitcnt lgkmcnt(0)
	global_store_dwordx4 v[6:7], v[2:5], off
	v_lshl_add_u64 v[6:7], s[4:5], 0, v[136:137]
	s_nop 0
	v_add_u32_e32 v2, v8, v187
	ds_read_b128 v[2:5], v2
	v_lshl_add_u64 v[6:7], v[6:7], 0, v[152:153]
	s_waitcnt lgkmcnt(0)
	global_store_dwordx4 v[6:7], v[2:5], off
	s_nop 1
	v_add_u32_e32 v2, v8, v189
	ds_read_b128 v[2:5], v2
	v_lshl_add_u64 v[6:7], s[4:5], 0, v[138:139]
	v_lshl_add_u64 v[6:7], v[6:7], 0, v[152:153]
	s_mov_b64 s[4:5], 0
	s_waitcnt lgkmcnt(0)
	global_store_dwordx4 v[6:7], v[2:5], off
	s_waitcnt lgkmcnt(0)
	s_cbranch_vccnz .LBB0_317

; __device__ __forceinline__ unsigned cvtpk(float lo, float hi) { f32x2_t v = {lo, hi}; bf16x2_t b = __builtin_convertvector(v, bf16x2_t); return __builtin_bit_cast(unsigned, b); }
; __device__ __forceinline__ int crow(int r, int hi) { return (r & 3) + 8 * (r >> 2) + 4 * hi; }
; template <class BIAS>
; __device__ __forceinline__ void attn_tiles(char* shm, const UnitIO& io, int t_begin, int t_end, const BIAS& B, int tid) {
;     ...
;     float rli[16];
; #pragma unroll
;     for (int r = 0; r < 16; ++r) rli[r] = io.norm ? __builtin_amdgcn_rcpf(wsf[32 + crow(r, hi)]) : 1.0f;
;     if (!io.norm && hi == 0) io.L[(long)r32 * io.lstride] = l_reg;
;     { bf16* stg = (bf16*)(shm + LDS_OST) + wid * 2048;
; #pragma unroll
;       for (int r = 0; r < 16; ++r) { const int orow = crow(r, hi);
; #pragma unroll
;           for (int d0 = 0; d0 < 2; ++d0) stg[orow * 64 + d0 * 32 + r32] = (bf16)(cvtpk(o[d0][r] * rli[r], 0.f) & 0xffffu); }
;       asm volatile("s_waitcnt lgkmcnt(0)" ::: "memory");
; #pragma unroll
;       for (int i = 0; i < 4; ++i) { const int row = i * 8 + (lane >> 3), ch = lane & 7; const u32x4 v = *(const u32x4*)(stg + row * 64 + ch * 8); __builtin_nontemporal_store(v, (u32x4*)(io.O + (long)row * io.ostride + ch * 8)); } }
.LBB0_318:
	s_or_b64 exec, exec, s[42:43]
	s_waitcnt lgkmcnt(0)
	v_lshl_add_u32 v10, v163, 2, s21
	ds_read_b128 v[2:5], v10 offset:128
	ds_read_b128 v[6:9], v10 offset:160
	s_lshl_b64 s[22:23], s[34:35], 1
	v_readlane_b32 s26, v254, 59
	s_add_u32 s22, s26, s22
	v_readlane_b32 s26, v254, 63
	s_addc_u32 s23, s26, s23
	s_lshl_b32 s20, s20, 1
	s_waitcnt lgkmcnt(1)
	v_rcp_f32_e32 v11, v2
	s_add_u32 s34, s22, s20
	s_addc_u32 s35, s23, 0
	s_lshl_b32 s20, s54, 12
	s_add_i32 s20, s20, 0x10800
	v_rcp_f32_e32 v12, v3
	v_rcp_f32_e32 v13, v4
	v_rcp_f32_e32 v14, v5
	s_waitcnt lgkmcnt(0)
	v_rcp_f32_e32 v15, v6
	ds_read_b128 v[2:5], v10 offset:192
	v_rcp_f32_e32 v16, v7
	v_rcp_f32_e32 v17, v8
	v_rcp_f32_e32 v18, v9
	ds_read_b128 v[6:9], v10 offset:224
	v_mul_f32_e32 v10, v202, v11
	v_lshl_or_b32 v19, v179, 1, s20
	v_cvt_pk_bf16_f32 v10, v10, s0
	v_lshl_add_u32 v19, v146, 1, v19
	ds_write_b16 v19, v10
	v_mul_f32_e32 v10, v211, v11
	v_cvt_pk_bf16_f32 v10, v10, s0
	ds_write_b16 v19, v10 offset:64
	v_mul_f32_e32 v10, v200, v12
	v_cvt_pk_bf16_f32 v10, v10, s0
	ds_write_b16 v19, v10 offset:128
	v_mul_f32_e32 v10, v210, v12
	v_cvt_pk_bf16_f32 v10, v10, s0
	ds_write_b16 v19, v10 offset:192
	v_mul_f32_e32 v10, v198, v13
	v_cvt_pk_bf16_f32 v10, v10, s0
	ds_write_b16 v19, v10 offset:256
	v_mul_f32_e32 v10, v209, v13
	v_cvt_pk_bf16_f32 v10, v10, s0
	ds_write_b16 v19, v10 offset:320
	v_mul_f32_e32 v10, v196, v14
	v_cvt_pk_bf16_f32 v10, v10, s0
	ds_write_b16 v19, v10 offset:384
	v_mul_f32_e32 v10, v208, v14
	v_cvt_pk_bf16_f32 v10, v10, s0
	ds_write_b16 v19, v10 offset:448
	v_mul_f32_e32 v10, v176, v15
	v_cvt_pk_bf16_f32 v10, v10, s0
	ds_write_b16 v19, v10 offset:1024
	v_mul_f32_e32 v10, v207, v15
	v_cvt_pk_bf16_f32 v10, v10, s0
	ds_write_b16 v19, v10 offset:1088
	v_mul_f32_e32 v10, v174, v16
	v_cvt_pk_bf16_f32 v10, v10, s0
	ds_write_b16 v19, v10 offset:1152
	v_mul_f32_e32 v10, v206, v16
	v_cvt_pk_bf16_f32 v10, v10, s0
	ds_write_b16 v19, v10 offset:1216
	v_mul_f32_e32 v10, v172, v17
	v_cvt_pk_bf16_f32 v10, v10, s0
	ds_write_b16 v19, v10 offset:1280
	v_mul_f32_e32 v10, v205, v17
	v_cvt_pk_bf16_f32 v10, v10, s0
	s_waitcnt lgkmcnt(14)
	v_rcp_f32_e32 v2, v2
	ds_write_b16 v19, v10 offset:1344
	v_mul_f32_e32 v10, v170, v18
	v_cvt_pk_bf16_f32 v10, v10, s0
	v_rcp_f32_e32 v3, v3
	ds_write_b16 v19, v10 offset:1408
	v_mul_f32_e32 v10, v204, v18
	v_cvt_pk_bf16_f32 v10, v10, s0
	ds_write_b16 v19, v10 offset:1472
	v_mul_f32_e32 v10, v169, v2
	v_mul_f32_e32 v2, v203, v2
	v_cvt_pk_bf16_f32 v2, v2, s0
	v_rcp_f32_e32 v4, v4
	ds_write_b16 v19, v2 offset:2112
	v_mul_f32_e32 v2, v167, v3
	v_cvt_pk_bf16_f32 v2, v2, s0
	ds_write_b16 v19, v2 offset:2176
	v_mul_f32_e32 v2, v201, v3
	v_cvt_pk_bf16_f32 v2, v2, s0
	v_rcp_f32_e32 v5, v5
	ds_write_b16 v19, v2 offset:2240
	v_mul_f32_e32 v2, v153, v4
	v_cvt_pk_bf16_f32 v2, v2, s0
	ds_write_b16 v19, v2 offset:2304
	v_mul_f32_e32 v2, v199, v4
	v_cvt_pk_bf16_f32 v2, v2, s0
	s_waitcnt lgkmcnt(14)
	v_rcp_f32_e32 v6, v6
	ds_write_b16 v19, v2 offset:2368
	v_mul_f32_e32 v2, v149, v5
	v_cvt_pk_bf16_f32 v2, v2, s0
	ds_write_b16 v19, v2 offset:2432
	v_mul_f32_e32 v2, v197, v5
	v_cvt_pk_bf16_f32 v2, v2, s0
	v_rcp_f32_e32 v7, v7
	ds_write_b16 v19, v2 offset:2496
	v_mul_f32_e32 v2, v168, v6
	v_cvt_pk_bf16_f32 v2, v2, s0
	ds_write_b16 v19, v2 offset:3072
	v_mul_f32_e32 v2, v177, v6
	v_cvt_pk_bf16_f32 v2, v2, s0
	v_rcp_f32_e32 v8, v8
	ds_write_b16 v19, v2 offset:3136
	v_mul_f32_e32 v2, v166, v7
	v_cvt_pk_bf16_f32 v2, v2, s0
	ds_write_b16 v19, v2 offset:3200
	v_mul_f32_e32 v2, v175, v7
	v_cvt_pk_bf16_f32 v2, v2, s0
	v_rcp_f32_e32 v9, v9
	ds_write_b16 v19, v2 offset:3264
	v_mul_f32_e32 v2, v151, v8
	v_cvt_pk_bf16_f32 v2, v2, s0
	ds_write_b16 v19, v2 offset:3328
	v_mul_f32_e32 v2, v173, v8
	v_cvt_pk_bf16_f32 v2, v2, s0
	ds_write_b16 v19, v2 offset:3392
	v_mul_f32_e32 v2, v139, v9
	v_cvt_pk_bf16_f32 v2, v2, s0
	ds_write_b16 v19, v2 offset:3456
	v_mul_f32_e32 v2, v171, v9
	v_cvt_pk_bf16_f32 v10, v10, s0
	v_cvt_pk_bf16_f32 v2, v2, s0
	ds_write_b16 v19, v10 offset:2048
	ds_write_b16 v19, v2 offset:3520
	v_or_b32_e32 v8, s20, v152
	s_waitcnt lgkmcnt(0)
	v_add_u32_e32 v2, v8, v183
	ds_read_b128 v[2:5], v2
	v_lshl_add_u64 v[6:7], s[34:35], 0, v[0:1]
	v_mov_b32_e32 v153, v1
	v_lshl_add_u64 v[6:7], v[6:7], 0, v[152:153]
	v_mov_b32_e32 v135, v1
	s_waitcnt lgkmcnt(0)
	global_store_dwordx4 v[6:7], v[2:5], off offset:512
	v_lshl_add_u64 v[6:7], s[34:35], 0, v[134:135]
	v_lshl_add_u64 v[6:7], v[6:7], 0, v[152:153]
	v_add_u32_e32 v2, v8, v185
	ds_read_b128 v[2:5], v2
	v_mov_b32_e32 v137, v1
	v_mov_b32_e32 v139, v1
	s_add_i32 s50, s50, 1
	s_add_i32 s52, s52, 5
	s_waitcnt lgkmcnt(0)
	global_store_dwordx4 v[6:7], v[2:5], off offset:512
	v_lshl_add_u64 v[6:7], s[34:35], 0, v[136:137]
	v_lshl_add_u64 v[6:7], v[6:7], 0, v[152:153]
	v_add_u32_e32 v2, v8, v187
	ds_read_b128 v[2:5], v2
	s_cmp_lg_u32 s50, 3
	s_waitcnt lgkmcnt(0)
	global_store_dwordx4 v[6:7], v[2:5], off offset:512
	s_nop 1
	v_add_u32_e32 v2, v8, v189
	ds_read_b128 v[2:5], v2
	v_lshl_add_u64 v[6:7], s[34:35], 0, v[138:139]
	v_lshl_add_u64 v[6:7], v[6:7], 0, v[152:153]
	s_waitcnt lgkmcnt(0)
	global_store_dwordx4 v[6:7], v[2:5], off offset:512
	s_waitcnt lgkmcnt(0)
	s_cbranch_scc0 .LBB0_361

; __device__ __forceinline__ unsigned cvtpk(float lo, float hi) { f32x2_t v = {lo, hi}; bf16x2_t b = __builtin_convertvector(v, bf16x2_t); return __builtin_bit_cast(unsigned, b); }
; __device__ __forceinline__ int crow(int r, int hi) { return (r & 3) + 8 * (r >> 2) + 4 * hi; }
; template <class BIAS>
; __device__ __forceinline__ void attn_tiles(char* shm, const UnitIO& io, int t_begin, int t_end, const BIAS& B, int tid) {
;     ...
;     float rli[16];
; #pragma unroll
;     for (int r = 0; r < 16; ++r) rli[r] = io.norm ? __builtin_amdgcn_rcpf(wsf[32 + crow(r, hi)]) : 1.0f;
;     if (!io.norm && hi == 0) io.L[(long)r32 * io.lstride] = l_reg;
;     { bf16* stg = (bf16*)(shm + LDS_OST) + wid * 2048;
; #pragma unroll
;       for (int r = 0; r < 16; ++r) { const int orow = crow(r, hi);
; #pragma unroll
;           for (int d0 = 0; d0 < 2; ++d0) stg[orow * 64 + d0 * 32 + r32] = (bf16)(cvtpk(o[d0][r] * rli[r], 0.f) & 0xffffu); }
;       asm volatile("s_waitcnt lgkmcnt(0)" ::: "memory");
; #pragma unroll
;       for (int i = 0; i < 4; ++i) { const int row = i * 8 + (lane >> 3), ch = lane & 7; const u32x4 v = *(const u32x4*)(stg + row * 64 + ch * 8); __builtin_nontemporal_store(v, (u32x4*)(io.O + (long)row * io.ostride + ch * 8)); } }
.LBB0_362:
	s_or_b64 exec, exec, s[56:57]
	s_and_b64 s[56:57], s[64:65], exec
	s_movk_i32 s56, 0x1800
	v_readlane_b32 s2, v190, 7
	s_cselect_b32 s64, 0x600, s56
	s_mul_hi_u32 s56, s2, 0x1800000
	s_mul_i32 s57, s2, 0x1800000
	v_readlane_b32 s2, v255, 23
	s_add_u32 s57, s2, s57
	v_readlane_b32 s2, v255, 24
	s_mul_i32 s65, s67, 0x300
	s_mul_hi_u32 s67, s66, 0x300
	s_addc_u32 s56, s2, s56
	s_add_i32 s67, s67, s65
	s_mul_i32 s65, s66, 0x300
	s_add_u32 s57, s57, s65
	v_readlane_b32 s2, v190, 9
	s_addc_u32 s65, s56, s67
	s_lshl_b32 s56, s2, 1
	s_add_u32 s56, s57, s56
	s_addc_u32 s57, s65, 0
	s_lshl_b32 s65, s76, 12
	s_add_i32 s65, s65, 0x10800
	v_cvt_pk_bf16_f32 v0, v2, s0
	v_lshl_or_b32 v2, v179, 1, s65
	v_lshl_add_u32 v2, v146, 1, v2
	ds_write_b16 v2, v0
	v_cvt_pk_bf16_f32 v0, v18, s0
	ds_write_b16 v2, v0 offset:64
	v_cvt_pk_bf16_f32 v0, v3, s0
	ds_write_b16 v2, v0 offset:128
	v_cvt_pk_bf16_f32 v0, v19, s0
	ds_write_b16 v2, v0 offset:192
	v_cvt_pk_bf16_f32 v0, v4, s0
	ds_write_b16 v2, v0 offset:256
	v_cvt_pk_bf16_f32 v0, v20, s0
	ds_write_b16 v2, v0 offset:320
	v_cvt_pk_bf16_f32 v0, v5, s0
	ds_write_b16 v2, v0 offset:384
	v_cvt_pk_bf16_f32 v0, v21, s0
	ds_write_b16 v2, v0 offset:448
	v_cvt_pk_bf16_f32 v0, v6, s0
	ds_write_b16 v2, v0 offset:1024
	v_cvt_pk_bf16_f32 v0, v22, s0
	ds_write_b16 v2, v0 offset:1088
	v_cvt_pk_bf16_f32 v0, v7, s0
	ds_write_b16 v2, v0 offset:1152
	v_cvt_pk_bf16_f32 v0, v23, s0
	ds_write_b16 v2, v0 offset:1216
	v_cvt_pk_bf16_f32 v0, v8, s0
	ds_write_b16 v2, v0 offset:1280
	v_cvt_pk_bf16_f32 v0, v24, s0
	ds_write_b16 v2, v0 offset:1344
	v_cvt_pk_bf16_f32 v0, v9, s0
	ds_write_b16 v2, v0 offset:1408
	v_cvt_pk_bf16_f32 v0, v25, s0
	ds_write_b16 v2, v0 offset:1472
	v_cvt_pk_bf16_f32 v0, v10, s0
	ds_write_b16 v2, v0 offset:2048
	v_cvt_pk_bf16_f32 v0, v26, s0
	ds_write_b16 v2, v0 offset:2112
	v_cvt_pk_bf16_f32 v0, v11, s0
	ds_write_b16 v2, v0 offset:2176
	v_cvt_pk_bf16_f32 v0, v27, s0
	ds_write_b16 v2, v0 offset:2240
	v_cvt_pk_bf16_f32 v0, v12, s0
	ds_write_b16 v2, v0 offset:2304
	v_cvt_pk_bf16_f32 v0, v28, s0
	ds_write_b16 v2, v0 offset:2368
	v_cvt_pk_bf16_f32 v0, v13, s0
	ds_write_b16 v2, v0 offset:2432
	v_cvt_pk_bf16_f32 v0, v29, s0
	ds_write_b16 v2, v0 offset:2496
	v_cvt_pk_bf16_f32 v0, v14, s0
	ds_write_b16 v2, v0 offset:3072
	v_cvt_pk_bf16_f32 v0, v30, s0
	ds_write_b16 v2, v0 offset:3136
	v_cvt_pk_bf16_f32 v0, v15, s0
	ds_write_b16 v2, v0 offset:3200
	v_cvt_pk_bf16_f32 v0, v31, s0
	ds_write_b16 v2, v0 offset:3264
	v_cvt_pk_bf16_f32 v0, v16, s0
	ds_write_b16 v2, v0 offset:3328
	v_cvt_pk_bf16_f32 v0, v32, s0
	ds_write_b16 v2, v0 offset:3392
	v_cvt_pk_bf16_f32 v0, v17, s0
	ds_write_b16 v2, v0 offset:3456
	v_cvt_pk_bf16_f32 v0, v33, s0
	ds_write_b16 v2, v0 offset:3520
	v_or_b32_e32 v8, s65, v152
	s_waitcnt lgkmcnt(0)
	v_add_u32_e32 v0, v8, v183
	s_and_b64 s[62:63], s[62:63], exec
	ds_read_b128 v[2:5], v0
	s_cselect_b32 s62, 0x180, s64
	v_mul_u32_u24_e32 v0, s62, v182
	v_lshlrev_b32_e32 v0, 1, v0
	v_lshl_add_u64 v[6:7], s[56:57], 0, v[0:1]
	v_mov_b32_e32 v153, v1
	v_lshl_add_u64 v[6:7], v[6:7], 0, v[152:153]
	s_waitcnt lgkmcnt(0)
	global_store_dwordx4 v[6:7], v[2:5], off
	v_add_u32_e32 v0, v8, v185
	ds_read_b128 v[2:5], v0
	v_mul_u32_u24_e32 v0, s62, v184
	v_lshlrev_b32_e32 v0, 1, v0
	v_lshl_add_u64 v[6:7], s[56:57], 0, v[0:1]
	v_lshl_add_u64 v[6:7], v[6:7], 0, v[152:153]
	s_waitcnt lgkmcnt(0)
	global_store_dwordx4 v[6:7], v[2:5], off
	v_add_u32_e32 v0, v8, v187
	ds_read_b128 v[2:5], v0
	v_mul_u32_u24_e32 v0, s62, v186
	v_lshlrev_b32_e32 v0, 1, v0
	v_lshl_add_u64 v[6:7], s[56:57], 0, v[0:1]
	v_lshl_add_u64 v[6:7], v[6:7], 0, v[152:153]
	s_waitcnt lgkmcnt(0)
	global_store_dwordx4 v[6:7], v[2:5], off
	v_add_u32_e32 v0, v8, v189
	ds_read_b128 v[2:5], v0
	v_mul_u32_u24_e32 v0, s62, v188
	v_lshlrev_b32_e32 v0, 1, v0
	v_lshl_add_u64 v[6:7], s[56:57], 0, v[0:1]
	v_lshl_add_u64 v[6:7], v[6:7], 0, v[152:153]
	s_waitcnt lgkmcnt(0)
	global_store_dwordx4 v[6:7], v[2:5], off
	s_waitcnt lgkmcnt(0)
	v_readlane_b32 s3, v254, 10
	s_cmp_eq_u32 s100, 0
	s_cbranch_scc1 .Ldl_ret
	s_branch .LBB0_393
